# fp8 GEMM LDS operand reads made bank-conflict-free in moe1, moe2 and glu (16-byte halves of each lane's 32-byte K slice swapped for odd k-groups, both MFMA operands alike; f32 accumulate unchanged)
# baseline (speedup 1.0000x reference)
.LBB0_1653:
	v_readfirstlane_b32 s24, v4
	s_mul_i32 s7, s7, s24
	s_add_u32 s42, s48, 0x29110100
	s_mul_hi_u32 s7, s24, s7
	s_addc_u32 s43, s49, 0
	s_abs_i32 s23, s10
	s_add_i32 s24, s24, s7
	s_mul_hi_u32 s7, s23, s24
	s_mul_i32 s24, s7, s6
	s_sub_i32 s23, s23, s24
	s_ashr_i32 s1, s10, 31
	s_add_i32 s24, s7, 1
	s_sub_i32 s30, s23, s6
	s_cmp_ge_u32 s23, s6
	s_cselect_b32 s7, s24, s7
	s_cselect_b32 s23, s30, s23
	s_add_i32 s24, s7, 1
	s_cmp_ge_u32 s23, s6
	s_cselect_b32 s6, s24, s7
	s_xor_b32 s6, s6, s1
	s_sub_i32 s66, s6, s1
	s_lshl_b32 s1, s22, 5
	s_and_b32 s68, s1, 0x60
	s_lshl_b32 s67, s21, 6
	s_lshl_b32 s21, s21, 13
	s_lshl_b32 s22, s68, 7
	s_add_i32 s69, s19, 0x18400
	s_add_i32 s70, s19, 0x1a400
	v_lshl_add_u64 v[0:1], v[0:1], 0, s[26:27]
	s_mov_b32 m0, s69
	s_add_u32 s44, s48, 0x17110180
	s_waitcnt vmcnt(2)
	s_barrier
	global_load_lds_dwordx4 v[0:1], off
	v_lshl_add_u64 v[0:1], v[2:3], 0, s[26:27]
	s_mov_b32 m0, s70
	s_addc_u32 s45, s49, 0
	s_add_i32 s71, s19, 0x8400
	s_add_i32 s72, s19, 0xa400
	v_mov_b32_e32 v199, v113
	global_load_lds_dwordx4 v[0:1], off
	v_lshl_add_u64 v[0:1], s[44:45], 0, v[112:113]
	s_mov_b32 m0, s71
	s_add_u32 s6, s2, 0x40080
	global_load_lds_dwordx4 v[0:1], off
	v_lshl_add_u64 v[0:1], s[44:45], 0, v[198:199]
	s_mov_b32 m0, s72
	s_addc_u32 s7, s3, 0
	s_add_i32 s73, s19, 0x1c400
	global_load_lds_dwordx4 v[0:1], off
	v_lshl_add_u64 v[0:1], s[6:7], 0, v[196:197]
	s_mov_b32 m0, s73
	s_add_i32 s74, s19, 0x1e400
	global_load_lds_dwordx4 v[0:1], off
	v_lshl_add_u64 v[0:1], s[6:7], 0, v[194:195]
	s_mov_b32 m0, s74
	v_lshlrev_b32_e32 v3, 2, v223
	global_load_lds_dwordx4 v[0:1], off
	v_lshlrev_b32_e32 v0, 1, v249
	v_and_b32_e32 v0, 32, v0
	v_lshlrev_b32_e32 v2, 5, v249
	v_and_b32_e32 v3, 32, v3
	s_sext_i32_i8 s1, s4
	v_lshl_or_b32 v1, v223, 6, v0
	v_and_b32_e32 v2, 0x400, v2
	v_bitop3_b32 v0, v7, v3, v0 bitop3:0x36
	s_waitcnt vmcnt(6)
	s_add_i32 s4, s22, 0
	s_add_i32 s21, s21, 0
	v_add3_u32 v0, s4, v0, v2
	v_xad_u32 v1, v1, v3, s21
	s_cmpk_lt_u32 s5, 0x100
	s_mov_b32 s75, 0
	v_add_u32_e32 v230, 0x10400, v0
	v_add_u32_e32 v231, 0x14400, v0
	v_add_u32_e32 v232, 0x18400, v0
	v_add_u32_e32 v233, 0x1c400, v0
	s_cselect_b64 s[46:47], -1, 0
	s_ashr_i32 s76, s67, 31
	v_add_u32_e32 v234, 0x10410, v0
	v_add_u32_e32 v236, 0x10c10, v0
	v_add_u32_e32 v237, 0x14410, v0
	v_add_u32_e32 v238, 0x14c00, v0
	v_add_u32_e32 v239, 0x14c10, v0
	v_add_u32_e32 v240, 0x18410, v0
	v_add_u32_e32 v241, 0x18c00, v0
	v_add_u32_e32 v242, 0x18c10, v0
	v_add_u32_e32 v243, 0x1c410, v0
	v_add_u32_e32 v244, 0x1cc00, v0
	v_add_u32_e32 v245, 0x1cc10, v0
	v_add_u32_e32 v246, v1, v2
	v_mbcnt_lo_u32_b32 v235, -1, 0
	v_mbcnt_hi_u32_b32 v235, -1, v235
	v_and_b32_e32 v235, 16, v235
	v_add_u32_e32 v230, v230, v235
	v_add_u32_e32 v231, v231, v235
	v_add_u32_e32 v232, v232, v235
	v_add_u32_e32 v233, v233, v235
	v_add_u32_e32 v238, v238, v235
	v_add_u32_e32 v241, v241, v235
	v_add_u32_e32 v244, v244, v235
	v_sub_u32_e32 v234, v234, v235
	v_sub_u32_e32 v236, v236, v235
	v_sub_u32_e32 v237, v237, v235
	v_sub_u32_e32 v239, v239, v235
	v_sub_u32_e32 v240, v240, v235
	v_sub_u32_e32 v242, v242, v235
	v_sub_u32_e32 v243, v243, v235
	v_sub_u32_e32 v245, v245, v235
	v_add_u32_e32 v246, v246, v235
	v_lshlrev_b32_e32 v235, 1, v235
	v_sub_u32_e32 v235, v246, v235
	s_barrier
	s_branch .LBB0_1656

.LBB0_1660:
	s_waitcnt vmcnt(8)
	s_add_u32 s6, s2, 0x80
	s_waitcnt lgkmcnt(0)
	s_addc_u32 s7, s3, 0
	s_and_b64 s[4:5], s[4:5], exec
	s_cselect_b32 s7, s39, s7
	s_cselect_b32 s6, s38, s6
	s_cselect_b32 s5, s21, s24
	s_cselect_b32 s4, s22, s23
	s_barrier
	s_setprio 1
	s_waitcnt lgkmcnt(0)
	v_mfma_scale_f32_16x16x128_f8f6f4 v[190:193], v[24:31], v[56:63], v[190:193], v216, v216 op_sel_hi:[0,0,0]
	v_mfma_scale_f32_16x16x128_f8f6f4 v[186:189], v[16:23], v[56:63], v[186:189], v216, v216 op_sel_hi:[0,0,0]
	v_mfma_scale_f32_16x16x128_f8f6f4 v[178:181], v[24:31], v[48:55], v[178:181], v216, v216 op_sel_hi:[0,0,0]
	v_mfma_scale_f32_16x16x128_f8f6f4 v[170:173], v[16:23], v[48:55], v[170:173], v216, v216 op_sel_hi:[0,0,0]
	v_mfma_scale_f32_16x16x128_f8f6f4 v[162:165], v[24:31], v[40:47], v[162:165], v216, v216 op_sel_hi:[0,0,0]
	v_mfma_scale_f32_16x16x128_f8f6f4 v[154:157], v[16:23], v[40:47], v[154:157], v216, v216 op_sel_hi:[0,0,0]
	v_mfma_scale_f32_16x16x128_f8f6f4 v[146:149], v[24:31], v[32:39], v[146:149], v216, v216 op_sel_hi:[0,0,0]
	v_mfma_scale_f32_16x16x128_f8f6f4 v[138:141], v[16:23], v[32:39], v[138:141], v216, v216 op_sel_hi:[0,0,0]
	s_setprio 0
	s_setprio 1
	v_mfma_scale_f32_16x16x128_f8f6f4 v[182:185], v[0:7], v[56:63], v[182:185], v216, v216 op_sel_hi:[0,0,0]
	v_mfma_scale_f32_16x16x128_f8f6f4 v[174:177], v[8:15], v[56:63], v[174:177], v216, v216 op_sel_hi:[0,0,0]
	v_mfma_scale_f32_16x16x128_f8f6f4 v[166:169], v[0:7], v[48:55], v[166:169], v216, v216 op_sel_hi:[0,0,0]
	v_mfma_scale_f32_16x16x128_f8f6f4 v[158:161], v[8:15], v[48:55], v[158:161], v216, v216 op_sel_hi:[0,0,0]
	v_mfma_scale_f32_16x16x128_f8f6f4 v[150:153], v[0:7], v[40:47], v[150:153], v216, v216 op_sel_hi:[0,0,0]
	v_mfma_scale_f32_16x16x128_f8f6f4 v[142:145], v[8:15], v[40:47], v[142:145], v216, v216 op_sel_hi:[0,0,0]
	v_mfma_scale_f32_16x16x128_f8f6f4 v[134:137], v[0:7], v[32:39], v[134:137], v216, v216 op_sel_hi:[0,0,0]
	v_mfma_scale_f32_16x16x128_f8f6f4 v[130:133], v[8:15], v[32:39], v[130:133], v216, v216 op_sel_hi:[0,0,0]
	s_setprio 0
	s_barrier
	s_mov_b32 m0, s28
	v_lshl_add_u64 v[250:251], s[4:5], 0, v[196:197]
	s_add_u32 s78, s4, 0x40000
	ds_read_b128 v[32:35], v246 offset:17408
	ds_read_b128 v[36:39], v235 offset:17424
	ds_read_b128 v[40:43], v246 offset:19456
	ds_read_b128 v[44:47], v235 offset:19472
	ds_read_b128 v[48:51], v246 offset:21504
	ds_read_b128 v[52:55], v235 offset:21520
	ds_read_b128 v[56:59], v246 offset:23552
	ds_read_b128 v[60:63], v235 offset:23568
	global_load_lds_dwordx4 v[250:251], off
	v_lshl_add_u64 v[252:253], s[4:5], 0, v[194:195]
	s_mov_b32 m0, s29
	s_addc_u32 s79, s5, 0
	global_load_lds_dwordx4 v[252:253], off
	v_lshl_add_u64 v[220:221], s[78:79], 0, v[196:197]
	s_mov_b32 m0, s60
	v_mov_b32_e32 v199, v113
	global_load_lds_dwordx4 v[220:221], off
	v_lshl_add_u64 v[220:221], s[78:79], 0, v[194:195]
	s_mov_b32 m0, s61
	v_lshl_add_u64 v[224:225], s[6:7], 0, v[198:199]
	global_load_lds_dwordx4 v[220:221], off
	s_mov_b32 m0, s62
	v_lshl_add_u64 v[220:221], s[6:7], 0, v[112:113]
	global_load_lds_dwordx4 v112, s[6:7]
	s_mov_b32 m0, s63
	s_nop 0
	global_load_lds_dwordx4 v198, s[6:7]
	s_waitcnt vmcnt(8)
	s_waitcnt lgkmcnt(0)
	s_barrier
	s_setprio 1
	s_waitcnt lgkmcnt(0)
	v_mfma_scale_f32_16x16x128_f8f6f4 v[126:129], v[24:31], v[32:39], v[126:129], v216, v216 op_sel_hi:[0,0,0]
	v_mfma_scale_f32_16x16x128_f8f6f4 v[122:125], v[16:23], v[32:39], v[122:125], v216, v216 op_sel_hi:[0,0,0]
	v_mfma_scale_f32_16x16x128_f8f6f4 v[114:117], v[24:31], v[40:47], v[114:117], v216, v216 op_sel_hi:[0,0,0]
	v_mfma_scale_f32_16x16x128_f8f6f4 v[104:107], v[16:23], v[40:47], v[104:107], v216, v216 op_sel_hi:[0,0,0]
	v_mfma_scale_f32_16x16x128_f8f6f4 v[96:99], v[24:31], v[48:55], v[96:99], v216, v216 op_sel_hi:[0,0,0]
	v_mfma_scale_f32_16x16x128_f8f6f4 v[88:91], v[16:23], v[48:55], v[88:91], v216, v216 op_sel_hi:[0,0,0]
	v_mfma_scale_f32_16x16x128_f8f6f4 v[80:83], v[24:31], v[56:63], v[80:83], v216, v216 op_sel_hi:[0,0,0]
	v_mfma_scale_f32_16x16x128_f8f6f4 v[72:75], v[16:23], v[56:63], v[72:75], v216, v216 op_sel_hi:[0,0,0]
	s_setprio 0
	s_setprio 1
	v_mfma_scale_f32_16x16x128_f8f6f4 v[118:121], v[0:7], v[32:39], v[118:121], v216, v216 op_sel_hi:[0,0,0]
	v_mfma_scale_f32_16x16x128_f8f6f4 v[108:111], v[8:15], v[32:39], v[108:111], v216, v216 op_sel_hi:[0,0,0]
	v_mfma_scale_f32_16x16x128_f8f6f4 v[100:103], v[0:7], v[40:47], v[100:103], v216, v216 op_sel_hi:[0,0,0]
	v_mfma_scale_f32_16x16x128_f8f6f4 v[92:95], v[8:15], v[40:47], v[92:95], v216, v216 op_sel_hi:[0,0,0]
	v_mfma_scale_f32_16x16x128_f8f6f4 v[84:87], v[0:7], v[48:55], v[84:87], v216, v216 op_sel_hi:[0,0,0]
	v_mfma_scale_f32_16x16x128_f8f6f4 v[76:79], v[8:15], v[48:55], v[76:79], v216, v216 op_sel_hi:[0,0,0]
	v_mfma_scale_f32_16x16x128_f8f6f4 v[68:71], v[0:7], v[56:63], v[68:71], v216, v216 op_sel_hi:[0,0,0]
	v_mfma_scale_f32_16x16x128_f8f6f4 v[64:67], v[8:15], v[56:63], v[64:67], v216, v216 op_sel_hi:[0,0,0]
	s_setprio 0
	s_barrier
	ds_read_b128 v[4:7], v240
	ds_read_b128 v[8:11], v241
	ds_read_b128 v[0:3], v232
	ds_read_b128 v[16:19], v233
	ds_read_b128 v[12:15], v242
	ds_read_b128 v[20:23], v243
	ds_read_b128 v[24:27], v244
	ds_read_b128 v[28:31], v245
	s_mov_b32 m0, s64
	v_lshl_add_u64 v[210:211], s[6:7], 0, v[210:211]
	ds_read_b128 v[32:35], v246 offset:33792
	ds_read_b128 v[36:39], v235 offset:33808
	ds_read_b128 v[40:43], v246 offset:35840
	ds_read_b128 v[44:47], v235 offset:35856
	ds_read_b128 v[48:51], v246 offset:37888
	ds_read_b128 v[52:55], v235 offset:37904
	ds_read_b128 v[56:59], v246 offset:39936
	ds_read_b128 v[60:63], v235 offset:39952
	global_load_lds_dwordx4 v[210:211], off
	v_lshl_add_u64 v[208:209], s[6:7], 0, v[208:209]
	s_mov_b32 m0, s65
	s_nop 0
	global_load_lds_dwordx4 v[208:209], off
	s_waitcnt vmcnt(8)
	s_waitcnt lgkmcnt(0)
	s_barrier
	s_setprio 1
	s_waitcnt lgkmcnt(0)
	v_mfma_scale_f32_16x16x128_f8f6f4 v[190:193], v[0:7], v[32:39], v[190:193], v216, v216 op_sel_hi:[0,0,0]
	v_mfma_scale_f32_16x16x128_f8f6f4 v[186:189], v[8:15], v[32:39], v[186:189], v216, v216 op_sel_hi:[0,0,0]
	v_mfma_scale_f32_16x16x128_f8f6f4 v[178:181], v[0:7], v[40:47], v[178:181], v216, v216 op_sel_hi:[0,0,0]
	v_mfma_scale_f32_16x16x128_f8f6f4 v[170:173], v[8:15], v[40:47], v[170:173], v216, v216 op_sel_hi:[0,0,0]
	v_mfma_scale_f32_16x16x128_f8f6f4 v[162:165], v[0:7], v[48:55], v[162:165], v216, v216 op_sel_hi:[0,0,0]
	v_mfma_scale_f32_16x16x128_f8f6f4 v[154:157], v[8:15], v[48:55], v[154:157], v216, v216 op_sel_hi:[0,0,0]
	v_mfma_scale_f32_16x16x128_f8f6f4 v[146:149], v[0:7], v[56:63], v[146:149], v216, v216 op_sel_hi:[0,0,0]
	v_mfma_scale_f32_16x16x128_f8f6f4 v[138:141], v[8:15], v[56:63], v[138:141], v216, v216 op_sel_hi:[0,0,0]
	s_setprio 0
	s_setprio 1
	v_mfma_scale_f32_16x16x128_f8f6f4 v[182:185], v[16:23], v[32:39], v[182:185], v216, v216 op_sel_hi:[0,0,0]
	v_mfma_scale_f32_16x16x128_f8f6f4 v[174:177], v[24:31], v[32:39], v[174:177], v216, v216 op_sel_hi:[0,0,0]
	v_mfma_scale_f32_16x16x128_f8f6f4 v[166:169], v[16:23], v[40:47], v[166:169], v216, v216 op_sel_hi:[0,0,0]
	v_mfma_scale_f32_16x16x128_f8f6f4 v[158:161], v[24:31], v[40:47], v[158:161], v216, v216 op_sel_hi:[0,0,0]
	v_mfma_scale_f32_16x16x128_f8f6f4 v[150:153], v[16:23], v[48:55], v[150:153], v216, v216 op_sel_hi:[0,0,0]
	v_mfma_scale_f32_16x16x128_f8f6f4 v[142:145], v[24:31], v[48:55], v[142:145], v216, v216 op_sel_hi:[0,0,0]
	v_mfma_scale_f32_16x16x128_f8f6f4 v[134:137], v[16:23], v[56:63], v[134:137], v216, v216 op_sel_hi:[0,0,0]
	v_mfma_scale_f32_16x16x128_f8f6f4 v[130:133], v[24:31], v[56:63], v[130:133], v216, v216 op_sel_hi:[0,0,0]
	s_setprio 0
	s_barrier
	s_mov_b32 m0, s69
	v_lshl_add_u64 v[208:209], v[250:251], 0, s[26:27]
	s_add_u32 s4, s4, 0x40080
	ds_read_b128 v[32:35], v246 offset:50176
	ds_read_b128 v[36:39], v235 offset:50192
	ds_read_b128 v[40:43], v246 offset:52224
	ds_read_b128 v[44:47], v235 offset:52240
	ds_read_b128 v[48:51], v246 offset:54272
	ds_read_b128 v[52:55], v235 offset:54288
	ds_read_b128 v[56:59], v246 offset:56320
	ds_read_b128 v[60:63], v235 offset:56336
	global_load_lds_dwordx4 v[208:209], off
	v_lshl_add_u64 v[208:209], v[252:253], 0, s[26:27]
	s_mov_b32 m0, s70
	s_addc_u32 s5, s5, 0
	global_load_lds_dwordx4 v[208:209], off
	v_lshl_add_u64 v[208:209], s[4:5], 0, v[196:197]
	s_mov_b32 m0, s73
	s_nop 0
	global_load_lds_dwordx4 v[208:209], off
	v_lshl_add_u64 v[208:209], s[4:5], 0, v[194:195]
	s_mov_b32 m0, s74
	s_nop 0
	global_load_lds_dwordx4 v[208:209], off
	v_lshl_add_u64 v[208:209], v[220:221], 0, s[26:27]
	s_mov_b32 m0, s71
	s_nop 0
	global_load_lds_dwordx4 v[208:209], off
	v_lshl_add_u64 v[208:209], v[224:225], 0, s[26:27]
	s_mov_b32 m0, s72
	s_nop 0
	global_load_lds_dwordx4 v[208:209], off
	s_waitcnt vmcnt(8)
	s_waitcnt lgkmcnt(0)
	s_barrier
	s_setprio 1
	s_waitcnt lgkmcnt(0)
	v_mfma_scale_f32_16x16x128_f8f6f4 v[126:129], v[0:7], v[32:39], v[126:129], v216, v216 op_sel_hi:[0,0,0]
	v_mfma_scale_f32_16x16x128_f8f6f4 v[122:125], v[8:15], v[32:39], v[122:125], v216, v216 op_sel_hi:[0,0,0]
	v_mfma_scale_f32_16x16x128_f8f6f4 v[114:117], v[0:7], v[40:47], v[114:117], v216, v216 op_sel_hi:[0,0,0]
	v_mfma_scale_f32_16x16x128_f8f6f4 v[104:107], v[8:15], v[40:47], v[104:107], v216, v216 op_sel_hi:[0,0,0]
	v_mfma_scale_f32_16x16x128_f8f6f4 v[96:99], v[0:7], v[48:55], v[96:99], v216, v216 op_sel_hi:[0,0,0]
	v_mfma_scale_f32_16x16x128_f8f6f4 v[88:91], v[8:15], v[48:55], v[88:91], v216, v216 op_sel_hi:[0,0,0]
	v_mfma_scale_f32_16x16x128_f8f6f4 v[80:83], v[0:7], v[56:63], v[80:83], v216, v216 op_sel_hi:[0,0,0]
	v_mfma_scale_f32_16x16x128_f8f6f4 v[72:75], v[8:15], v[56:63], v[72:75], v216, v216 op_sel_hi:[0,0,0]
	s_setprio 0
	s_setprio 1
	v_mfma_scale_f32_16x16x128_f8f6f4 v[118:121], v[16:23], v[32:39], v[118:121], v216, v216 op_sel_hi:[0,0,0]
	v_mfma_scale_f32_16x16x128_f8f6f4 v[108:111], v[24:31], v[32:39], v[108:111], v216, v216 op_sel_hi:[0,0,0]
	v_mfma_scale_f32_16x16x128_f8f6f4 v[100:103], v[16:23], v[40:47], v[100:103], v216, v216 op_sel_hi:[0,0,0]
	v_mfma_scale_f32_16x16x128_f8f6f4 v[92:95], v[24:31], v[40:47], v[92:95], v216, v216 op_sel_hi:[0,0,0]
	v_mfma_scale_f32_16x16x128_f8f6f4 v[84:87], v[16:23], v[48:55], v[84:87], v216, v216 op_sel_hi:[0,0,0]
	v_mfma_scale_f32_16x16x128_f8f6f4 v[76:79], v[24:31], v[48:55], v[76:79], v216, v216 op_sel_hi:[0,0,0]
	v_mfma_scale_f32_16x16x128_f8f6f4 v[68:71], v[16:23], v[56:63], v[68:71], v216, v216 op_sel_hi:[0,0,0]
	v_mfma_scale_f32_16x16x128_f8f6f4 v[64:67], v[24:31], v[56:63], v[64:67], v216, v216 op_sel_hi:[0,0,0]
	s_setprio 0
	s_barrier
	s_add_i32 s30, s30, 2
	s_add_u32 s23, s23, 0x100
	s_addc_u32 s24, s24, 0
	s_add_u32 s2, s2, 0x100
	s_addc_u32 s3, s3, 0
	s_cmp_gt_u32 s30, 13
	s_cbranch_scc1 .LBB0_1663
.LBB0_1661:
	ds_read_b128 v[28:31], v234
	ds_read_b128 v[16:19], v230 offset:2048
	ds_read_b128 v[24:27], v230
	ds_read_b128 v[0:3], v231
	ds_read_b128 v[20:23], v236
	ds_read_b128 v[4:7], v237
	ds_read_b128 v[8:11], v238
	ds_read_b128 v[12:15], v239
	s_cmp_eq_u32 s30, 12
	s_cselect_b64 s[4:5], -1, 0
	s_add_i32 m0, s19, 0xc400
	ds_read_b128 v[56:59], v246 offset:1024
	ds_read_b128 v[60:63], v235 offset:1040
	ds_read_b128 v[48:51], v246 offset:3072
	ds_read_b128 v[52:55], v235 offset:3088
	ds_read_b128 v[40:43], v246 offset:5120
	ds_read_b128 v[44:47], v235 offset:5136
	ds_read_b128 v[32:35], v246 offset:7168
	ds_read_b128 v[36:39], v235 offset:7184
	global_load_lds_dwordx4 v200, s[2:3]
	s_add_i32 m0, s19, 0xe400
	s_and_b64 s[6:7], s[54:55], s[4:5]
	global_load_lds_dwordx4 v202, s[2:3]
	s_andn2_b64 vcc, exec, s[6:7]
	s_cbranch_vccz .LBB0_1659
	v_mov_b32_e32 v201, v113
	v_mov_b32_e32 v203, v113
	v_mov_b64_e32 v[208:209], v[202:203]
	v_mov_b64_e32 v[210:211], v[200:201]
	s_branch .LBB0_1660
